# re-measure: 16x16x32 latent attention body with softmax exp/add interleaved into P.V (best so far)
# speedup vs baseline: 1.0693x; 1.0082x over previous
; #define SBAR() __builtin_amdgcn_sched_barrier(0)
; #define RESC(a) do { if (__any((a) < 1.f)) { if (hi == 0) al_l[r32] = (a); asm volatile("s_waitcnt lgkmcnt(0)" ::: "memory"); \
;     for (int d = 0; d < 4; ++d) for (int r = 0; r < 16; ++r) o[d][r] *= al_l[crow(r, hi)]; } } while (0)
; #define RESC(a) do { if (__any((a) < 1.f)) { if (hi == 0) al_l[r32] = (a); asm volatile("s_waitcnt lgkmcnt(0)" ::: "memory"); \
;     for (int d = 0; d < 4; ++d) for (int r = 0; r < 16; ++r) o[d][r] *= al_l[crow(r, hi)]; } } while (0)
; #define ATT_SYNC(jn) do { ATT_WAIT_BAR(); if ((jn) < NT) ATT_DMA((jn), (jn) & 3); } while (0)
; __device__ __forceinline__ void attn_dma_body(const bf16_t* __restrict__ Qb, int ldq, int tpos0, const float* __restrict__ rope, const float* __restrict__ qgain, ...
;     ...
;   for (int j = 1; j + 1 < NT; j += 2) {
;     { SBAR(); qkt(pB0, pB1, (const bf16_t*)(lds + (j & 3) * SHM_SLOT), qr, r32, hi);
;       finishSM(pA0, pA1, alA, l_reg, pa0, pa1, pa2, pa3); s16x4 va[8]; pv_rd<0>(va, vb0 + ((j - 1) & 3) * (int)SHM_SLOT); SBAR();
;       if (!lead) ATT_SYNC(j + 2);
;       pv_d0_pre(o, vb0 + ((j - 1) & 3) * (int)SHM_SLOT, va, pa0, pa1, pa2, pa3); partialSM(pB0, pB1, m_reg, mnB, alB);
;       if (lead) ATT_SYNC(j + 2);
;       RESC(alB); }
;     { SBAR(); qkt(pA0, pA1, (const bf16_t*)(lds + ((j + 1) & 3) * SHM_SLOT), qr, r32, hi);
;       finishSM(pB0, pB1, alB, l_reg, pa0, pa1, pa2, pa3); s16x4 va[8]; pv_rd<0>(va, vb0 + (j & 3) * (int)SHM_SLOT); SBAR();
;       if (!lead) ATT_SYNC(j + 3);
;       pv_d0_pre(o, vb0 + (j & 3) * (int)SHM_SLOT, va, pa0, pa1, pa2, pa3); partialSM(pA0, pA1, m_reg, mnA, alA);
;       if (lead) ATT_SYNC(j + 3);
;       RESC(alA); }
.Lf16_se_nl:
.Lf16_a:
	s_waitcnt lgkmcnt(6)
	v_mfma_f32_16x16x32_bf16 v[2:5], v[214:217], v[130:133], v[2:5]
	v_exp_f32_e32 v66, v66
	v_mfma_f32_16x16x32_bf16 v[6:9], v[214:217], v[138:141], v[6:9]
	v_exp_f32_e32 v67, v67
	ds_read_b64_tr_b16 v[230:231], v193 offset:1024
	ds_read_b64_tr_b16 v[232:233], v193 offset:5120
	s_waitcnt lgkmcnt(6)
	v_mfma_f32_16x16x32_bf16 v[10:13], v[218:221], v[130:133], v[10:13]
	v_exp_f32_e32 v68, v68
	v_add_f32_e32 v182, v182, v66
	v_mfma_f32_16x16x32_bf16 v[14:17], v[218:221], v[138:141], v[14:17]
	v_exp_f32_e32 v69, v69
	v_add_f32_e32 v182, v182, v67
	ds_read_b64_tr_b16 v[234:235], v194 offset:1024
	ds_read_b64_tr_b16 v[236:237], v194 offset:5120
	s_waitcnt lgkmcnt(6)
	v_mfma_f32_16x16x32_bf16 v[18:21], v[222:225], v[130:133], v[18:21]
	v_exp_f32_e32 v70, v70
	v_add_f32_e32 v182, v182, v68
	v_mfma_f32_16x16x32_bf16 v[22:25], v[222:225], v[138:141], v[22:25]
	v_exp_f32_e32 v71, v71
	v_add_f32_e32 v182, v182, v69
	ds_read_b64_tr_b16 v[238:239], v193 offset:1536
	ds_read_b64_tr_b16 v[240:241], v193 offset:5632
	s_waitcnt lgkmcnt(6)
	v_mfma_f32_16x16x32_bf16 v[26:29], v[226:229], v[130:133], v[26:29]
	v_exp_f32_e32 v72, v72
	v_add_f32_e32 v195, v195, v70
	v_mfma_f32_16x16x32_bf16 v[30:33], v[226:229], v[138:141], v[30:33]
	v_exp_f32_e32 v73, v73
	v_add_f32_e32 v195, v195, v71
	ds_read_b64_tr_b16 v[242:243], v194 offset:1536
	ds_read_b64_tr_b16 v[244:245], v194 offset:5632
	s_waitcnt lgkmcnt(6)
	v_mfma_f32_16x16x32_bf16 v[34:37], v[230:233], v[130:133], v[34:37]
	v_exp_f32_e32 v74, v74
	v_add_f32_e32 v195, v195, v72
	v_mfma_f32_16x16x32_bf16 v[38:41], v[230:233], v[138:141], v[38:41]
	v_exp_f32_e32 v75, v75
	v_add_f32_e32 v195, v195, v73
	ds_read_b64_tr_b16 v[214:215], v193 offset:8192
	ds_read_b64_tr_b16 v[216:217], v193 offset:12288
	s_waitcnt lgkmcnt(6)
	v_mfma_f32_16x16x32_bf16 v[42:45], v[234:237], v[130:133], v[42:45]
	v_exp_f32_e32 v76, v76
	v_add_f32_e32 v182, v182, v74
	v_mfma_f32_16x16x32_bf16 v[46:49], v[234:237], v[138:141], v[46:49]
	v_exp_f32_e32 v77, v77
	v_add_f32_e32 v182, v182, v75
	ds_read_b64_tr_b16 v[218:219], v194 offset:8192
	ds_read_b64_tr_b16 v[220:221], v194 offset:12288
	s_waitcnt lgkmcnt(6)
	v_mfma_f32_16x16x32_bf16 v[50:53], v[238:241], v[130:133], v[50:53]
	v_exp_f32_e32 v78, v78
	v_add_f32_e32 v182, v182, v76
	v_mfma_f32_16x16x32_bf16 v[54:57], v[238:241], v[138:141], v[54:57]
	v_exp_f32_e32 v79, v79
	v_add_f32_e32 v182, v182, v77
	ds_read_b64_tr_b16 v[222:223], v193 offset:8704
	ds_read_b64_tr_b16 v[224:225], v193 offset:12800
	s_waitcnt lgkmcnt(6)
	v_mfma_f32_16x16x32_bf16 v[58:61], v[242:245], v[130:133], v[58:61]
	v_exp_f32_e32 v80, v80
	v_add_f32_e32 v195, v195, v78
	v_mfma_f32_16x16x32_bf16 v[62:65], v[242:245], v[138:141], v[62:65]
	v_exp_f32_e32 v81, v81
	v_add_f32_e32 v195, v195, v79
	ds_read_b64_tr_b16 v[226:227], v194 offset:8704
	ds_read_b64_tr_b16 v[228:229], v194 offset:12800
	s_waitcnt lgkmcnt(6)
	v_mfma_f32_16x16x32_bf16 v[2:5], v[214:217], v[134:137], v[2:5]
	v_exp_f32_e32 v82, v82
	v_add_f32_e32 v195, v195, v80
	v_mfma_f32_16x16x32_bf16 v[6:9], v[214:217], v[142:145], v[6:9]
	v_exp_f32_e32 v83, v83
	v_add_f32_e32 v195, v195, v81
	ds_read_b64_tr_b16 v[230:231], v193 offset:9216
	ds_read_b64_tr_b16 v[232:233], v193 offset:13312
	s_waitcnt lgkmcnt(6)
	v_mfma_f32_16x16x32_bf16 v[10:13], v[218:221], v[134:137], v[10:13]
	v_exp_f32_e32 v84, v84
	v_add_f32_e32 v182, v182, v82
	v_mfma_f32_16x16x32_bf16 v[14:17], v[218:221], v[142:145], v[14:17]
	v_exp_f32_e32 v85, v85
	v_add_f32_e32 v182, v182, v83
	ds_read_b64_tr_b16 v[234:235], v194 offset:9216
	ds_read_b64_tr_b16 v[236:237], v194 offset:13312
	s_waitcnt lgkmcnt(6)
	v_mfma_f32_16x16x32_bf16 v[18:21], v[222:225], v[134:137], v[18:21]
	v_exp_f32_e32 v86, v86
	v_add_f32_e32 v182, v182, v84
	v_mfma_f32_16x16x32_bf16 v[22:25], v[222:225], v[142:145], v[22:25]
	v_exp_f32_e32 v87, v87
	v_add_f32_e32 v182, v182, v85
	ds_read_b64_tr_b16 v[238:239], v193 offset:9728
	ds_read_b64_tr_b16 v[240:241], v193 offset:13824
	s_waitcnt lgkmcnt(6)
	v_mfma_f32_16x16x32_bf16 v[26:29], v[226:229], v[134:137], v[26:29]
	v_exp_f32_e32 v88, v88
	v_add_f32_e32 v195, v195, v86
	v_mfma_f32_16x16x32_bf16 v[30:33], v[226:229], v[142:145], v[30:33]
	v_exp_f32_e32 v89, v89
	v_add_f32_e32 v195, v195, v87
	ds_read_b64_tr_b16 v[242:243], v194 offset:9728
	ds_read_b64_tr_b16 v[244:245], v194 offset:13824
	s_waitcnt lgkmcnt(6)
	v_mfma_f32_16x16x32_bf16 v[34:37], v[230:233], v[134:137], v[34:37]
	v_exp_f32_e32 v90, v90
	v_add_f32_e32 v195, v195, v88
	v_mfma_f32_16x16x32_bf16 v[38:41], v[230:233], v[142:145], v[38:41]
	v_exp_f32_e32 v91, v91
	v_add_f32_e32 v195, v195, v89
	s_waitcnt lgkmcnt(4)
	v_mfma_f32_16x16x32_bf16 v[42:45], v[234:237], v[134:137], v[42:45]
	v_exp_f32_e32 v92, v92
	v_add_f32_e32 v182, v182, v90
	v_mfma_f32_16x16x32_bf16 v[46:49], v[234:237], v[142:145], v[46:49]
	v_exp_f32_e32 v93, v93
	v_add_f32_e32 v182, v182, v91
	s_waitcnt lgkmcnt(2)
	v_mfma_f32_16x16x32_bf16 v[50:53], v[238:241], v[134:137], v[50:53]
	v_exp_f32_e32 v94, v94
	v_add_f32_e32 v182, v182, v92
	v_mfma_f32_16x16x32_bf16 v[54:57], v[238:241], v[142:145], v[54:57]
	v_exp_f32_e32 v95, v95
	v_add_f32_e32 v182, v182, v93
	s_waitcnt lgkmcnt(0)
	v_mfma_f32_16x16x32_bf16 v[58:61], v[242:245], v[134:137], v[58:61]
	v_exp_f32_e32 v96, v96
	v_add_f32_e32 v195, v195, v94
	v_mfma_f32_16x16x32_bf16 v[62:65], v[242:245], v[142:145], v[62:65]
	v_exp_f32_e32 v97, v97
	v_add_f32_e32 v195, v195, v95
	s_cmp_lt_u32 s42, 4
	s_cbranch_scc0 .Lf16_b
	s_cmp_ge_u32 s97, 131
	s_cbranch_scc1 .Lf16_se_l
	s_waitcnt vmcnt(0) lgkmcnt(0)
	s_barrier
	s_cmp_ge_u32 s97, 130
	s_cbranch_scc1 .Lf16_se_l
	s_add_i32 s6, s36, 0x10000
	s_and_b32 s6, s6, 0x18000
	s_add_i32 s6, s6, s96
	s_mov_b32 m0, s6
	s_nop 0
	global_load_lds_dwordx4 v170, s[2:3]
	s_add_i32 m0, s6, 0x2000
	s_nop 0
	global_load_lds_dwordx4 v172, s[2:3]
	s_add_i32 m0, s6, 0x4000
	s_nop 0
	global_load_lds_dwordx4 v171, s[4:5]
	s_add_i32 m0, s6, 0x6000
	s_nop 0
	global_load_lds_dwordx4 v173, s[4:5]
	s_add_u32 s2, s2, 0x4000
	s_addc_u32 s3, s3, 0
	s_add_u32 s4, s4, 0x4000
	s_addc_u32 s5, s5, 0
; #define SBAR() __builtin_amdgcn_sched_barrier(0)
; #define RESC(a) do { if (__any((a) < 1.f)) { if (hi == 0) al_l[r32] = (a); asm volatile("s_waitcnt lgkmcnt(0)" ::: "memory"); \
;     for (int d = 0; d < 4; ++d) for (int r = 0; r < 16; ++r) o[d][r] *= al_l[crow(r, hi)]; } } while (0)
; #define RESC(a) do { if (__any((a) < 1.f)) { if (hi == 0) al_l[r32] = (a); asm volatile("s_waitcnt lgkmcnt(0)" ::: "memory"); \
;     for (int d = 0; d < 4; ++d) for (int r = 0; r < 16; ++r) o[d][r] *= al_l[crow(r, hi)]; } } while (0)
; #define ATT_SYNC(jn) do { ATT_WAIT_BAR(); if ((jn) < NT) ATT_DMA((jn), (jn) & 3); } while (0)
; __device__ __forceinline__ void attn_dma_body(const bf16_t* __restrict__ Qb, int ldq, int tpos0, const float* __restrict__ rope, const float* __restrict__ qgain, ...
;     ...
;   for (int j = 1; j + 1 < NT; j += 2) {
;     { SBAR(); qkt(pB0, pB1, (const bf16_t*)(lds + (j & 3) * SHM_SLOT), qr, r32, hi);
;       finishSM(pA0, pA1, alA, l_reg, pa0, pa1, pa2, pa3); s16x4 va[8]; pv_rd<0>(va, vb0 + ((j - 1) & 3) * (int)SHM_SLOT); SBAR();
;       if (!lead) ATT_SYNC(j + 2);
;       pv_d0_pre(o, vb0 + ((j - 1) & 3) * (int)SHM_SLOT, va, pa0, pa1, pa2, pa3); partialSM(pB0, pB1, m_reg, mnB, alB);
;       if (lead) ATT_SYNC(j + 2);
;       RESC(alB); }
;     { SBAR(); qkt(pA0, pA1, (const bf16_t*)(lds + ((j + 1) & 3) * SHM_SLOT), qr, r32, hi);
;       finishSM(pB0, pB1, alB, l_reg, pa0, pa1, pa2, pa3); s16x4 va[8]; pv_rd<0>(va, vb0 + (j & 3) * (int)SHM_SLOT); SBAR();
;       if (!lead) ATT_SYNC(j + 3);
;       pv_d0_pre(o, vb0 + (j & 3) * (int)SHM_SLOT, va, pa0, pa1, pa2, pa3); partialSM(pA0, pA1, m_reg, mnA, alA);
;       if (lead) ATT_SYNC(j + 3);
;       RESC(alA); }
;   }
;     ...
;   { SBAR(); qkt(pB0, pB1, (const bf16_t*)(lds + ((NT - 1) & 3) * SHM_SLOT), qr, r32, hi);
;     finishSM(pA0, pA1, alA, l_reg, pa0, pa1, pa2, pa3); SBAR();
;     pv_d0(o, vb0 + ((NT - 2) & 3) * (int)SHM_SLOT, pa0, pa1, pa2, pa3); partialSM(pB0, pB1, m_reg, mnB, alB);
;     RESC(alB);
;     finishSM(pB0, pB1, alB, l_reg, pa0, pa1, pa2, pa3); SBAR();
;     pv_d0(o, vb0 + ((NT - 1) & 3) * (int)SHM_SLOT, pa0, pa1, pa2, pa3); }
.Lf16_se_l:
.Lf16_b:
	v_add_f32_e32 v195, v195, v96
	v_add_f32_e32 v195, v195, v97
	v_cvt_pk_bf16_f32 v130, v66, v67
	v_cvt_pk_bf16_f32 v131, v68, v69
	v_cvt_pk_bf16_f32 v132, v74, v75
	v_cvt_pk_bf16_f32 v133, v76, v77
	v_cvt_pk_bf16_f32 v134, v82, v83
	v_cvt_pk_bf16_f32 v135, v84, v85
	v_cvt_pk_bf16_f32 v136, v90, v91
	v_cvt_pk_bf16_f32 v137, v92, v93
	v_cvt_pk_bf16_f32 v138, v70, v71
	v_cvt_pk_bf16_f32 v139, v72, v73
	v_cvt_pk_bf16_f32 v140, v78, v79
	v_cvt_pk_bf16_f32 v141, v80, v81
	v_cvt_pk_bf16_f32 v142, v86, v87
	v_cvt_pk_bf16_f32 v143, v88, v89
	v_cvt_pk_bf16_f32 v144, v94, v95
	v_cvt_pk_bf16_f32 v145, v96, v97
	s_add_i32 s97, s97, 1
	s_cmp_lt_u32 s97, 132
	s_cbranch_scc1 .Lf16_loop
	s_mov_b32 s37, 0x18000
	v_add_u32_e32 v193, s37, v191
	v_add_u32_e32 v194, s37, v192
	ds_read_b64_tr_b16 v[214:215], v193 offset:0
	ds_read_b64_tr_b16 v[216:217], v193 offset:4096
	ds_read_b64_tr_b16 v[218:219], v194 offset:0
	ds_read_b64_tr_b16 v[220:221], v194 offset:4096
	ds_read_b64_tr_b16 v[222:223], v193 offset:512
	ds_read_b64_tr_b16 v[224:225], v193 offset:4608
	ds_read_b64_tr_b16 v[226:227], v194 offset:512
	ds_read_b64_tr_b16 v[228:229], v194 offset:4608
	s_waitcnt lgkmcnt(6)
	v_mfma_f32_16x16x32_bf16 v[2:5], v[214:217], v[130:133], v[2:5]
	v_mfma_f32_16x16x32_bf16 v[6:9], v[214:217], v[138:141], v[6:9]
	ds_read_b64_tr_b16 v[230:231], v193 offset:1024
	ds_read_b64_tr_b16 v[232:233], v193 offset:5120
	s_waitcnt lgkmcnt(6)
	v_mfma_f32_16x16x32_bf16 v[10:13], v[218:221], v[130:133], v[10:13]
	v_mfma_f32_16x16x32_bf16 v[14:17], v[218:221], v[138:141], v[14:17]
	ds_read_b64_tr_b16 v[234:235], v194 offset:1024
	ds_read_b64_tr_b16 v[236:237], v194 offset:5120
	s_waitcnt lgkmcnt(6)
	v_mfma_f32_16x16x32_bf16 v[18:21], v[222:225], v[130:133], v[18:21]
	v_mfma_f32_16x16x32_bf16 v[22:25], v[222:225], v[138:141], v[22:25]
	ds_read_b64_tr_b16 v[238:239], v193 offset:1536
	ds_read_b64_tr_b16 v[240:241], v193 offset:5632
	s_waitcnt lgkmcnt(6)
	v_mfma_f32_16x16x32_bf16 v[26:29], v[226:229], v[130:133], v[26:29]
	v_mfma_f32_16x16x32_bf16 v[30:33], v[226:229], v[138:141], v[30:33]
	ds_read_b64_tr_b16 v[242:243], v194 offset:1536
	ds_read_b64_tr_b16 v[244:245], v194 offset:5632
	s_waitcnt lgkmcnt(6)
	v_mfma_f32_16x16x32_bf16 v[34:37], v[230:233], v[130:133], v[34:37]
	v_mfma_f32_16x16x32_bf16 v[38:41], v[230:233], v[138:141], v[38:41]
	ds_read_b64_tr_b16 v[214:215], v193 offset:8192
	ds_read_b64_tr_b16 v[216:217], v193 offset:12288
	s_waitcnt lgkmcnt(6)
	v_mfma_f32_16x16x32_bf16 v[42:45], v[234:237], v[130:133], v[42:45]
	v_mfma_f32_16x16x32_bf16 v[46:49], v[234:237], v[138:141], v[46:49]
	ds_read_b64_tr_b16 v[218:219], v194 offset:8192
	ds_read_b64_tr_b16 v[220:221], v194 offset:12288
	s_waitcnt lgkmcnt(6)
	v_mfma_f32_16x16x32_bf16 v[50:53], v[238:241], v[130:133], v[50:53]
	v_mfma_f32_16x16x32_bf16 v[54:57], v[238:241], v[138:141], v[54:57]
	ds_read_b64_tr_b16 v[222:223], v193 offset:8704
	ds_read_b64_tr_b16 v[224:225], v193 offset:12800
	s_waitcnt lgkmcnt(6)
	v_mfma_f32_16x16x32_bf16 v[58:61], v[242:245], v[130:133], v[58:61]
	v_mfma_f32_16x16x32_bf16 v[62:65], v[242:245], v[138:141], v[62:65]
	ds_read_b64_tr_b16 v[226:227], v194 offset:8704
	ds_read_b64_tr_b16 v[228:229], v194 offset:12800
	s_waitcnt lgkmcnt(6)
	v_mfma_f32_16x16x32_bf16 v[2:5], v[214:217], v[134:137], v[2:5]
	v_mfma_f32_16x16x32_bf16 v[6:9], v[214:217], v[142:145], v[6:9]
	ds_read_b64_tr_b16 v[230:231], v193 offset:9216
	ds_read_b64_tr_b16 v[232:233], v193 offset:13312
	s_waitcnt lgkmcnt(6)
	v_mfma_f32_16x16x32_bf16 v[10:13], v[218:221], v[134:137], v[10:13]
	v_mfma_f32_16x16x32_bf16 v[14:17], v[218:221], v[142:145], v[14:17]
	ds_read_b64_tr_b16 v[234:235], v194 offset:9216
	ds_read_b64_tr_b16 v[236:237], v194 offset:13312
	s_waitcnt lgkmcnt(6)
	v_mfma_f32_16x16x32_bf16 v[18:21], v[222:225], v[134:137], v[18:21]
	v_mfma_f32_16x16x32_bf16 v[22:25], v[222:225], v[142:145], v[22:25]
	ds_read_b64_tr_b16 v[238:239], v193 offset:9728
	ds_read_b64_tr_b16 v[240:241], v193 offset:13824
	s_waitcnt lgkmcnt(6)
	v_mfma_f32_16x16x32_bf16 v[26:29], v[226:229], v[134:137], v[26:29]
	v_mfma_f32_16x16x32_bf16 v[30:33], v[226:229], v[142:145], v[30:33]
	ds_read_b64_tr_b16 v[242:243], v194 offset:9728
	ds_read_b64_tr_b16 v[244:245], v194 offset:13824
	s_waitcnt lgkmcnt(6)
	v_mfma_f32_16x16x32_bf16 v[34:37], v[230:233], v[134:137], v[34:37]
	v_mfma_f32_16x16x32_bf16 v[38:41], v[230:233], v[142:145], v[38:41]
	s_waitcnt lgkmcnt(4)
	v_mfma_f32_16x16x32_bf16 v[42:45], v[234:237], v[134:137], v[42:45]
	v_mfma_f32_16x16x32_bf16 v[46:49], v[234:237], v[142:145], v[46:49]
	s_waitcnt lgkmcnt(2)
	v_mfma_f32_16x16x32_bf16 v[50:53], v[238:241], v[134:137], v[50:53]
	v_mfma_f32_16x16x32_bf16 v[54:57], v[238:241], v[142:145], v[54:57]
	s_waitcnt lgkmcnt(0)
	v_mfma_f32_16x16x32_bf16 v[58:61], v[242:245], v[134:137], v[58:61]
	v_mfma_f32_16x16x32_bf16 v[62:65], v[242:245], v[142:145], v[62:65]
	v_mov_b32_e32 v246, v182
	s_nop 1
	v_permlane32_swap_b32_e32 v182, v246
	v_add_f32_e32 v182, v182, v246
	v_mov_b32_e32 v246, v182
	s_nop 1
	v_permlane16_swap_b32_e32 v182, v246
	v_add_f32_e32 v182, v182, v246
	v_mov_b32_e32 v246, v195
	s_nop 1
	v_permlane32_swap_b32_e32 v195, v246
	v_add_f32_e32 v195, v195, v246
	v_mov_b32_e32 v246, v195
	s_nop 1
	v_permlane16_swap_b32_e32 v195, v246
	v_add_f32_e32 v195, v195, v246
	v_rcp_f32_e32 v182, v182
	v_rcp_f32_e32 v195, v195
	s_waitcnt lgkmcnt(0)
	s_barrier
; __device__ __forceinline__ unsigned f2bf(float f) { unsigned u = __builtin_bit_cast(unsigned, f); return (u + 0x7fffu + ((u >> 16) & 1u)) >> 16; }
; __device__ __forceinline__ int crow(int r, int hi) { return (r & 3) + 8 * (r >> 2) + 4 * hi; }
; #define ATT_WAIT_BAR() asm volatile("s_waitcnt vmcnt(0) lgkmcnt(0)\n\ts_barrier" ::: "memory")
; __device__ __forceinline__ void attn_dma_body(const bf16_t* __restrict__ Qb, int ldq, int tpos0, const float* __restrict__ rope, const float* __restrict__ qgain, ...
;     ...
;   if (hi == 0) li_l[r32] = l_reg; asm volatile("s_waitcnt lgkmcnt(0)" ::: "memory");
;   float rli[16];
; #pragma unroll
;   for (int r = 0; r < 16; ++r) rli[r] = __builtin_amdgcn_rcpf(li_l[crow(r, hi)]);
;   bf16_t* Ow = Ob + (long)(wid * QBLK) * LDO;
;   asm volatile("s_waitcnt lgkmcnt(0)\n\ts_barrier" ::: "memory");
;   { char* st = lds + wid * 8704;
; #pragma unroll
;     for (int r = 0; r < 16; ++r) { const int orow = crow(r, hi);
; #pragma unroll
;       for (int d0 = 0; d0 < 4; ++d0) *(bf16_t*)(st + orow * 272 + (d0 * 32 + r32) * 2) = (bf16_t)f2bf(o[d0][r] * rli[r]); }
;     asm volatile("s_waitcnt lgkmcnt(0)" ::: "memory");
; #pragma unroll
;     for (int i = 0; i < 8; ++i) { const int c = i * 64 + lane, row = c >> 4, cc = c & 15; const u32x4 v = *(const u32x4*)(st + row * 272 + cc * 16);
;       const bf16_t* gp = Ow + (long)row * LDO + cc * 8;
;       asm volatile("global_store_dwordx4 %0, %1, off sc1\n\ts_nop 1" :: "v"(gp), "v"(v) : "memory"); } }
;   ATT_WAIT_BAR();
	v_mul_u32_u24_e32 v84, 0x2200, v179
	v_and_b32_e32 v246, 15, v167
	v_lshrrev_b32_e32 v247, 4, v167
	v_mul_u32_u24_e32 v248, 0x110, v246
	v_add_u32_e32 v248, v248, v84
	v_lshl_add_u32 v248, v247, 3, v248
	v_mul_f32_e32 v2, v2, v182
	v_mul_f32_e32 v3, v3, v182
	v_mul_f32_e32 v4, v4, v182
	v_mul_f32_e32 v5, v5, v182
	v_cvt_pk_bf16_f32 v252, v2, v3
	v_cvt_pk_bf16_f32 v253, v4, v5
	ds_write_b64 v248, v[252:253] offset:0
	v_mul_f32_e32 v6, v6, v195
	v_mul_f32_e32 v7, v7, v195
	v_mul_f32_e32 v8, v8, v195
	v_mul_f32_e32 v9, v9, v195
	v_cvt_pk_bf16_f32 v254, v6, v7
	v_cvt_pk_bf16_f32 v255, v8, v9
	ds_write_b64 v248, v[254:255] offset:4352
	v_mul_f32_e32 v10, v10, v182
	v_mul_f32_e32 v11, v11, v182
	v_mul_f32_e32 v12, v12, v182
	v_mul_f32_e32 v13, v13, v182
	v_cvt_pk_bf16_f32 v252, v10, v11
	v_cvt_pk_bf16_f32 v253, v12, v13
	ds_write_b64 v248, v[252:253] offset:32
	v_mul_f32_e32 v14, v14, v195
	v_mul_f32_e32 v15, v15, v195
	v_mul_f32_e32 v16, v16, v195
	v_mul_f32_e32 v17, v17, v195
	v_cvt_pk_bf16_f32 v254, v14, v15
	v_cvt_pk_bf16_f32 v255, v16, v17
	ds_write_b64 v248, v[254:255] offset:4384
	v_mul_f32_e32 v18, v18, v182
	v_mul_f32_e32 v19, v19, v182
	v_mul_f32_e32 v20, v20, v182
	v_mul_f32_e32 v21, v21, v182
	v_cvt_pk_bf16_f32 v252, v18, v19
	v_cvt_pk_bf16_f32 v253, v20, v21
	ds_write_b64 v248, v[252:253] offset:64
	v_mul_f32_e32 v22, v22, v195
	v_mul_f32_e32 v23, v23, v195
	v_mul_f32_e32 v24, v24, v195
	v_mul_f32_e32 v25, v25, v195
	v_cvt_pk_bf16_f32 v254, v22, v23
	v_cvt_pk_bf16_f32 v255, v24, v25
	ds_write_b64 v248, v[254:255] offset:4416
	v_mul_f32_e32 v26, v26, v182
	v_mul_f32_e32 v27, v27, v182
	v_mul_f32_e32 v28, v28, v182
	v_mul_f32_e32 v29, v29, v182
	v_cvt_pk_bf16_f32 v252, v26, v27
	v_cvt_pk_bf16_f32 v253, v28, v29
	ds_write_b64 v248, v[252:253] offset:96
	v_mul_f32_e32 v30, v30, v195
	v_mul_f32_e32 v31, v31, v195
	v_mul_f32_e32 v32, v32, v195
	v_mul_f32_e32 v33, v33, v195
	v_cvt_pk_bf16_f32 v254, v30, v31
	v_cvt_pk_bf16_f32 v255, v32, v33
	ds_write_b64 v248, v[254:255] offset:4448
	v_mul_f32_e32 v34, v34, v182
	v_mul_f32_e32 v35, v35, v182
	v_mul_f32_e32 v36, v36, v182
	v_mul_f32_e32 v37, v37, v182
	v_cvt_pk_bf16_f32 v252, v34, v35
	v_cvt_pk_bf16_f32 v253, v36, v37
	ds_write_b64 v248, v[252:253] offset:128
	v_mul_f32_e32 v38, v38, v195
	v_mul_f32_e32 v39, v39, v195
	v_mul_f32_e32 v40, v40, v195
	v_mul_f32_e32 v41, v41, v195
	v_cvt_pk_bf16_f32 v254, v38, v39
	v_cvt_pk_bf16_f32 v255, v40, v41
	ds_write_b64 v248, v[254:255] offset:4480
	v_mul_f32_e32 v42, v42, v182
	v_mul_f32_e32 v43, v43, v182
	v_mul_f32_e32 v44, v44, v182
	v_mul_f32_e32 v45, v45, v182
	v_cvt_pk_bf16_f32 v252, v42, v43
	v_cvt_pk_bf16_f32 v253, v44, v45
	ds_write_b64 v248, v[252:253] offset:160
	v_mul_f32_e32 v46, v46, v195
	v_mul_f32_e32 v47, v47, v195
	v_mul_f32_e32 v48, v48, v195
	v_mul_f32_e32 v49, v49, v195
	v_cvt_pk_bf16_f32 v254, v46, v47
	v_cvt_pk_bf16_f32 v255, v48, v49
	ds_write_b64 v248, v[254:255] offset:4512
	v_mul_f32_e32 v50, v50, v182
	v_mul_f32_e32 v51, v51, v182
	v_mul_f32_e32 v52, v52, v182
	v_mul_f32_e32 v53, v53, v182
	v_cvt_pk_bf16_f32 v252, v50, v51
	v_cvt_pk_bf16_f32 v253, v52, v53
	ds_write_b64 v248, v[252:253] offset:192
	v_mul_f32_e32 v54, v54, v195
	v_mul_f32_e32 v55, v55, v195
	v_mul_f32_e32 v56, v56, v195
	v_mul_f32_e32 v57, v57, v195
	v_cvt_pk_bf16_f32 v254, v54, v55
	v_cvt_pk_bf16_f32 v255, v56, v57
	ds_write_b64 v248, v[254:255] offset:4544
	v_mul_f32_e32 v58, v58, v182
	v_mul_f32_e32 v59, v59, v182
	v_mul_f32_e32 v60, v60, v182
	v_mul_f32_e32 v61, v61, v182
	v_cvt_pk_bf16_f32 v252, v58, v59
	v_cvt_pk_bf16_f32 v253, v60, v61
	ds_write_b64 v248, v[252:253] offset:224
	v_mul_f32_e32 v62, v62, v195
	v_mul_f32_e32 v63, v63, v195
	v_mul_f32_e32 v64, v64, v195
	v_mul_f32_e32 v65, v65, v195
	v_cvt_pk_bf16_f32 v254, v62, v63
	v_cvt_pk_bf16_f32 v255, v64, v65
	ds_write_b64 v248, v[254:255] offset:4576
	s_waitcnt lgkmcnt(0)
	s_lshl_b64 s[6:7], s[70:71], 12
	s_add_u32 s6, s23, s6
	s_addc_u32 s7, s94, s7
	s_add_u32 s6, s6, s44
	s_addc_u32 s7, s7, s45
	v_ashrrev_i32_e32 v165, 31, v164
	v_lshlrev_b64 v[66:67], 12, v[164:165]
	v_lshl_add_u64 v[6:7], s[6:7], 0, v[66:67]
	v_lshlrev_b32_e32 v162, 4, v246
	v_lshl_add_u64 v[6:7], v[6:7], 0, v[162:163]
	v_lshlrev_b32_e32 v162, 12, v247
	v_lshl_add_u64 v[6:7], v[6:7], 0, v[162:163]
	v_mul_u32_u24_e32 v249, 0x110, v247
	v_add_u32_e32 v249, v249, v84
	v_lshl_add_u32 v249, v246, 4, v249
	ds_read_b128 v[10:13], v249 offset:0
	s_mov_b64 s[8:9], 0x0
	v_lshl_add_u64 v[8:9], v[6:7], 0, s[8:9]
	s_waitcnt lgkmcnt(0)
	global_store_dwordx4 v[8:9], v[10:13], off sc1
	s_nop 1
	ds_read_b128 v[14:17], v249 offset:1088
	s_mov_b64 s[8:9], 0x4000
	v_lshl_add_u64 v[8:9], v[6:7], 0, s[8:9]
	s_waitcnt lgkmcnt(0)
	global_store_dwordx4 v[8:9], v[14:17], off sc1
	s_nop 1
	ds_read_b128 v[10:13], v249 offset:2176
	s_mov_b64 s[8:9], 0x8000
	v_lshl_add_u64 v[8:9], v[6:7], 0, s[8:9]
	s_waitcnt lgkmcnt(0)
	global_store_dwordx4 v[8:9], v[10:13], off sc1
	s_nop 1
	ds_read_b128 v[14:17], v249 offset:3264
	s_mov_b64 s[8:9], 0xc000
	v_lshl_add_u64 v[8:9], v[6:7], 0, s[8:9]
	s_waitcnt lgkmcnt(0)
	global_store_dwordx4 v[8:9], v[14:17], off sc1
	s_nop 1
	ds_read_b128 v[10:13], v249 offset:4352
	s_mov_b64 s[8:9], 0x10000
	v_lshl_add_u64 v[8:9], v[6:7], 0, s[8:9]
	s_waitcnt lgkmcnt(0)
	global_store_dwordx4 v[8:9], v[10:13], off sc1
	s_nop 1
	ds_read_b128 v[14:17], v249 offset:5440
	s_mov_b64 s[8:9], 0x14000
	v_lshl_add_u64 v[8:9], v[6:7], 0, s[8:9]
	s_waitcnt lgkmcnt(0)
	global_store_dwordx4 v[8:9], v[14:17], off sc1
	s_nop 1
	ds_read_b128 v[10:13], v249 offset:6528
	s_mov_b64 s[8:9], 0x18000
	v_lshl_add_u64 v[8:9], v[6:7], 0, s[8:9]
	s_waitcnt lgkmcnt(0)
	global_store_dwordx4 v[8:9], v[10:13], off sc1
	s_nop 1
	ds_read_b128 v[14:17], v249 offset:7616
	s_mov_b64 s[8:9], 0x1c000
	v_lshl_add_u64 v[8:9], v[6:7], 0, s[8:9]
	s_waitcnt lgkmcnt(0)
	global_store_dwordx4 v[8:9], v[14:17], off sc1
	s_nop 1
	s_waitcnt vmcnt(0) lgkmcnt(0)
	s_barrier
	v_readlane_b32 s96, v250, 4
	v_readlane_b32 s97, v250, 5
	s_setprio 0
	s_branch .LBB0_437
